# baseline (speedup 1.0000x reference)
.LBB0_63:
	s_or_b64 exec, exec, s[2:3]
	v_lshrrev_b32_e32 v6, 2, v1
	v_lshrrev_b32_e32 v5, 4, v1
	v_and_b32_e32 v6, 8, v6
	s_mov_b32 s0, 0x1fffff0
	v_and_b32_e32 v4, 31, v1
	v_and_or_b32 v5, v5, s0, v6
	v_lshrrev_b32_e32 v1, 1, v1
	s_movk_i32 s0, 0x60
	v_and_or_b32 v1, v1, s0, v4
	v_lshl_or_b32 v4, v5, 7, v1
	v_ashrrev_i32_e32 v5, 31, v4
	v_lshl_add_u64 v[2:3], v[4:5], 2, v[2:3]
	global_load_dword v6, v[2:3], off offset:1024
	global_load_dword v7, v[2:3], off offset:1536
	global_load_dword v4, v[2:3], off offset:2048
	global_load_dword v5, v[2:3], off offset:3072
	global_load_dword v8, v[2:3], off offset:3584
	global_load_dword v9, v[2:3], off offset:2560
	global_load_dword v10, v[2:3], off
	global_load_dword v11, v[2:3], off offset:512
	v_ashrrev_i32_e32 v1, 31, v0
	v_lshl_add_u64 v[0:1], v[0:1], 4, s[4:5]
	s_waitcnt vmcnt(6)
	v_cvt_pk_f16_f32 v3, v6, v7
	s_waitcnt vmcnt(3)
	v_cvt_pk_f16_f32 v5, v5, v8
	s_waitcnt vmcnt(2)
	v_cvt_pk_f16_f32 v4, v4, v9
	s_waitcnt vmcnt(0)
	v_cvt_pk_f16_f32 v2, v10, v11
	global_store_dwordx4 v[0:1], v[2:5], off sc1
	s_endpgm
	s_nop 0
	s_nop 0
	s_nop 0
	s_nop 0
	s_nop 0
	s_nop 0
	s_nop 0
	s_nop 0
	s_nop 0
	s_nop 0
	s_nop 0
	s_nop 0
	s_nop 0
	s_nop 0
	s_nop 0
	s_nop 0
	s_nop 0
	s_nop 0
	s_nop 0
	s_nop 0
	s_nop 0
	s_nop 0
	s_nop 0
	s_nop 0
	s_nop 0
	s_nop 0
	s_nop 0
	s_nop 0
	s_nop 0
	s_nop 0
	s_nop 0
	s_nop 0
	s_nop 0
	s_nop 0
	s_nop 0
	s_nop 0
	s_nop 0
	s_nop 0
	s_nop 0
	s_nop 0
	s_nop 0
	s_nop 0
	s_nop 0
	s_nop 0
	s_nop 0
	s_nop 0
	s_nop 0
	s_nop 0
	s_nop 0
	s_nop 0
	s_nop 0
	s_nop 0
	s_nop 0
	s_nop 0
	s_nop 0
	s_nop 0
	s_nop 0
	s_nop 0
	s_nop 0
	s_nop 0
	s_nop 0
	s_nop 0
	s_nop 0
	s_nop 0
	s_nop 0
	s_nop 0
	s_nop 0
	s_nop 0
	s_nop 0
	s_nop 0
	s_nop 0
	s_nop 0
	s_nop 0
	s_nop 0
	s_nop 0
	s_nop 0
	s_nop 0
	s_nop 0
	s_nop 0
	s_nop 0
	s_nop 0
	s_nop 0
	s_nop 0
	s_nop 0
	s_nop 0
	s_nop 0
	s_nop 0
	s_nop 0
	s_nop 0
	s_nop 0
	s_nop 0
	s_nop 0
	s_nop 0
	s_nop 0
	s_nop 0
	s_nop 0
	s_nop 0
	s_nop 0
	s_nop 0
	s_nop 0
	s_nop 0
	s_nop 0
	s_nop 0
	s_nop 0
	s_nop 0
	s_nop 0
	s_nop 0
	s_nop 0
	s_nop 0
	s_nop 0
	s_nop 0
	s_nop 0
	s_nop 0
	s_nop 0
	s_nop 0
	s_nop 0
	s_nop 0
	s_nop 0
	s_nop 0
	s_nop 0
	s_nop 0
	s_nop 0
	s_nop 0
	s_nop 0
	s_nop 0
	s_nop 0
	s_nop 0
	s_nop 0
	s_nop 0
	s_nop 0
	s_nop 0
	s_nop 0
	s_nop 0
	s_nop 0
	s_nop 0
	s_nop 0
	s_nop 0
	s_nop 0
	s_nop 0
	s_nop 0
	s_nop 0
	s_nop 0
	s_nop 0
	s_nop 0
	s_nop 0
	s_nop 0
	s_nop 0
	s_nop 0
	s_nop 0
	s_nop 0
	s_nop 0
	s_nop 0
	s_nop 0
	s_nop 0
	s_nop 0
	s_nop 0
	s_nop 0
	s_nop 0
	s_nop 0
	s_nop 0
	s_nop 0
	s_nop 0
	s_nop 0
	s_nop 0
	s_nop 0
	s_nop 0
	s_nop 0
	s_nop 0
	s_nop 0
	s_nop 0
	s_nop 0
	s_nop 0
	s_nop 0
	s_nop 0
	s_nop 0
	s_nop 0
	s_nop 0
	s_nop 0
	s_nop 0
	s_nop 0
	s_nop 0
	s_nop 0
	s_nop 0
	s_nop 0
	s_nop 0
	s_nop 0
	s_nop 0
	s_nop 0
	s_nop 0
	s_nop 0
	s_nop 0
	s_nop 0
	s_nop 0
	s_nop 0
	s_nop 0
	s_nop 0
	s_nop 0
	s_nop 0
	s_nop 0
	s_nop 0
	s_nop 0
	s_nop 0
	s_nop 0
	s_nop 0
	s_nop 0
	s_nop 0
	s_nop 0
	s_nop 0
	s_nop 0
	s_nop 0
	s_nop 0
	s_nop 0
	s_nop 0
	s_nop 0
	s_nop 0
	s_nop 0
	s_nop 0
	s_nop 0
	s_nop 0
	s_nop 0
	s_nop 0
	s_nop 0
	s_nop 0
	s_nop 0
	s_nop 0
	s_nop 0
	s_nop 0
	s_nop 0
	s_nop 0
	s_nop 0
	s_nop 0
	s_nop 0
	s_nop 0
	s_nop 0
	s_nop 0
	s_nop 0
	s_nop 0
	s_nop 0
	s_nop 0
	s_nop 0
	s_nop 0
	s_nop 0
	s_nop 0
	s_nop 0
	s_nop 0
	s_nop 0
	s_nop 0
	s_nop 0
	s_nop 0
	s_nop 0
	s_nop 0
	s_nop 0
	s_nop 0
	s_nop 0
	s_nop 0
	s_nop 0
